# P0 w_in item loop: next item's addresses+loads issued during the current item's LDS transpose (2 items in flight per wave); stacked on route prefetch
# baseline (speedup 1.0000x reference)
.LBB0_7:
	v_writelane_b32 v254, s2, 7
	s_load_dwordx16 s[36:51], s[0:1], 0x80
	v_readlane_b32 s2, v254, 0
	s_lshr_b32 s2, s2, 6
	s_add_u32 s6, s28, 0x200000
	s_addc_u32 s7, s29, 0
	s_add_u32 s34, s28, 0x4eb00000
	s_addc_u32 s35, s29, 0
	s_cmp_lt_i32 s30, 1
	v_writelane_b32 v254, s2, 8
	s_cselect_b64 s[2:3], -1, 0
	s_cmp_gt_i32 s31, 0
	s_cselect_b64 s[4:5], -1, 0
	s_and_b64 s[8:9], s[2:3], s[4:5]
	s_andn2_b64 vcc, exec, s[8:9]
	s_cbranch_vccnz .LBB0_24
	s_lshl_b32 s2, s93, 3
	v_readlane_b32 s3, v254, 8
	s_add_i32 s10, s3, s2
	s_load_dword s2, s[0:1], 0xd0
	s_waitcnt lgkmcnt(0)
	s_lshl_b32 s12, s2, 3
	s_cmpk_gt_i32 s10, 0x303f
	s_cbranch_scc1 .LBB0_11
	v_readlane_b32 s2, v254, 8
	v_and_b32_e32 v1, 63, v0
	s_lshl_b32 s2, s2, 14
	v_lshrrev_b32_e32 v8, 3, v1
	v_lshlrev_b32_e32 v1, 2, v0
	s_add_i32 s2, s2, 0
	v_and_b32_e32 v2, 28, v1
	v_lshlrev_b32_e32 v4, 3, v0
	v_lshl_add_u32 v1, v2, 2, s2
	v_mul_u32_u24_e32 v7, 0x84, v8
	v_and_b32_e32 v6, 56, v4
	v_mov_b32_e32 v3, 0
	v_mul_u32_u24_e32 v4, 0x84, v6
	v_lshlrev_b32_e32 v5, 2, v8
	v_add_u32_e32 v17, v1, v7
	v_or_b32_e32 v9, 8, v8
	v_or_b32_e32 v10, 16, v8
	v_or_b32_e32 v11, 24, v8
	v_or_b32_e32 v12, 32, v8
	v_or_b32_e32 v13, 40, v8
	v_or_b32_e32 v14, 48, v8
	v_or_b32_e32 v15, 56, v8
	v_add3_u32 v16, s2, v4, v5
	s_lshl_b32 s2, s10, 5
	s_lshl_b32 s3, s12, 5
	s_mov_b32 s11, 0xc100
	v_mov_b64_e32 v[4:5], s[72:73]
	v_lshlrev_b32_e32 v2, 2, v2
	v_add_u32_e32 v18, 0x420, v17
	v_add_u32_e32 v19, 0x428, v17
	v_add_u32_e32 v20, 0x840, v17
	v_add_u32_e32 v21, 0x848, v17
	v_add_u32_e32 v22, 0xc60, v17
	v_add_u32_e32 v23, 0xc68, v17
	v_add_u32_e32 v24, 0x1080, v17
	v_add_u32_e32 v25, 0x1088, v17
	v_add_u32_e32 v26, 0x14a0, v17
	v_add_u32_e32 v27, 0x14a8, v17
	v_add_u32_e32 v28, 0x18c0, v17
	v_add_u32_e32 v29, 0x18c8, v17
	v_add_u32_e32 v30, 0x1ce0, v17
	v_add_u32_e32 v31, 0x1ce8, v17
	v_lshlrev_b32_e32 v6, 1, v6
	v_mov_b32_e32 v7, v3
	s_mov_b32 s13, s10
	s_mul_hi_i32 s4, s13, 0x15390949
	s_lshr_b32 s5, s4, 31
	s_ashr_i32 s4, s4, 5
	s_add_i32 s5, s4, s5
	s_lshl_b32 s4, s5, 6
	s_mulk_i32 s5, 0xcfc0
	s_add_i32 s14, s2, s5
	v_or_b32_e32 v1, s4, v8
	v_or_b32_e32 v34, s4, v9
	v_or_b32_e32 v36, s4, v10
	v_or_b32_e32 v38, s4, v11
	v_or_b32_e32 v40, s4, v12
	v_or_b32_e32 v42, s4, v13
	v_or_b32_e32 v44, s4, v14
	v_or_b32_e32 v46, s4, v15
	s_ashr_i32 s15, s14, 31
	v_mad_i64_i32 v[32:33], s[16:17], v1, s11, v[4:5]
	v_mad_i64_i32 v[34:35], s[16:17], v34, s11, v[4:5]
	v_mad_i64_i32 v[36:37], s[16:17], v36, s11, v[4:5]
	v_mad_i64_i32 v[38:39], s[16:17], v38, s11, v[4:5]
	v_mad_i64_i32 v[40:41], s[16:17], v40, s11, v[4:5]
	v_mad_i64_i32 v[42:43], s[16:17], v42, s11, v[4:5]
	v_mad_i64_i32 v[44:45], s[16:17], v44, s11, v[4:5]
	v_mad_i64_i32 v[46:47], s[16:17], v46, s11, v[4:5]
	s_lshl_b64 s[16:17], s[14:15], 2
	s_nop 0
	v_lshl_add_u64 v[32:33], v[32:33], 0, s[16:17]
	v_lshl_add_u64 v[34:35], v[34:35], 0, s[16:17]
	v_lshl_add_u64 v[36:37], v[36:37], 0, s[16:17]
	v_lshl_add_u64 v[38:39], v[38:39], 0, s[16:17]
	v_lshl_add_u64 v[40:41], v[40:41], 0, s[16:17]
	v_lshl_add_u64 v[42:43], v[42:43], 0, s[16:17]
	v_lshl_add_u64 v[44:45], v[44:45], 0, s[16:17]
	v_lshl_add_u64 v[46:47], v[46:47], 0, s[16:17]
	v_lshl_add_u64 v[32:33], v[32:33], 0, v[2:3]
	v_lshl_add_u64 v[48:49], v[34:35], 0, v[2:3]
	v_lshl_add_u64 v[50:51], v[36:37], 0, v[2:3]
	v_lshl_add_u64 v[52:53], v[38:39], 0, v[2:3]
	v_lshl_add_u64 v[54:55], v[40:41], 0, v[2:3]
	v_lshl_add_u64 v[56:57], v[42:43], 0, v[2:3]
	v_lshl_add_u64 v[58:59], v[44:45], 0, v[2:3]
	v_lshl_add_u64 v[60:61], v[46:47], 0, v[2:3]
	global_load_dwordx4 v[110:113], v[32:33], off
	s_nop 0
	global_load_dwordx4 v[114:117], v[48:49], off
	global_load_dwordx4 v[118:121], v[50:51], off
	global_load_dwordx4 v[122:125], v[52:53], off
	s_nop 0
	global_load_dwordx4 v[126:129], v[54:55], off
	s_nop 0
	global_load_dwordx4 v[130:133], v[56:57], off
	s_nop 0
	global_load_dwordx4 v[134:137], v[58:59], off
	s_nop 0
	global_load_dwordx4 v[138:141], v[60:61], off
	s_waitcnt vmcnt(0)
.LBB0_10:
	s_waitcnt vmcnt(4)
	ds_write2_b32 v17, v110, v111 offset1:1
	ds_write2_b32 v17, v112, v113 offset0:2 offset1:3
	ds_write2_b32 v18, v114, v115 offset1:1
	ds_write2_b32 v19, v116, v117 offset1:1
	ds_write2_b32 v20, v118, v119 offset1:1
	ds_write2_b32 v21, v120, v121 offset1:1
	ds_write2_b32 v22, v122, v123 offset1:1
	ds_write2_b32 v23, v124, v125 offset1:1
	ds_write2_b32 v24, v126, v127 offset1:1
	ds_write2_b32 v25, v128, v129 offset1:1
	ds_write2_b32 v26, v130, v131 offset1:1
	ds_write2_b32 v27, v132, v133 offset1:1
	ds_write2_b32 v28, v134, v135 offset1:1
	ds_write2_b32 v29, v136, v137 offset1:1
	ds_write2_b32 v30, v138, v139 offset1:1
	ds_write2_b32 v31, v140, v141 offset1:1
	v_add_u32_e32 v64, s14, v8
	v_ashrrev_i32_e32 v65, 31, v64
	v_add_u32_e32 v66, 8, v64
	v_add_u32_e32 v68, 16, v64
	v_add_u32_e32 v70, 24, v64
	s_ashr_i32 s5, s4, 31
	v_lshlrev_b64 v[64:65], 12, v[64:65]
	v_ashrrev_i32_e32 v67, 31, v66
	v_ashrrev_i32_e32 v69, 31, v68
	v_ashrrev_i32_e32 v71, 31, v70
	s_lshl_b64 s[4:5], s[4:5], 1
	v_lshl_add_u64 v[64:65], s[6:7], 0, v[64:65]
	v_lshlrev_b64 v[66:67], 12, v[66:67]
	v_lshlrev_b64 v[68:69], 12, v[68:69]
	v_lshlrev_b64 v[70:71], 12, v[70:71]
	v_lshl_add_u64 v[64:65], v[64:65], 0, s[4:5]
	v_lshl_add_u64 v[66:67], s[6:7], 0, v[66:67]
	v_lshl_add_u64 v[68:69], s[6:7], 0, v[68:69]
	v_lshl_add_u64 v[70:71], s[6:7], 0, v[70:71]
	v_lshl_add_u64 v[64:65], v[64:65], 0, v[6:7]
	v_lshl_add_u64 v[66:67], v[66:67], 0, s[4:5]
	v_lshl_add_u64 v[68:69], v[68:69], 0, s[4:5]
	v_lshl_add_u64 v[70:71], v[70:71], 0, s[4:5]
	v_lshl_add_u64 v[66:67], v[66:67], 0, v[6:7]
	v_lshl_add_u64 v[68:69], v[68:69], 0, v[6:7]
	v_lshl_add_u64 v[70:71], v[70:71], 0, v[6:7]
	s_add_i32 s13, s13, s12
	s_add_i32 s2, s2, s3
	s_cmpk_gt_i32 s13, 0x303f
	s_cselect_b32 s18, 1, 0
	s_cbranch_scc1 .Lp0i_nopf
	s_mul_hi_i32 s4, s13, 0x15390949
	s_lshr_b32 s5, s4, 31
	s_ashr_i32 s4, s4, 5
	s_add_i32 s5, s4, s5
	s_lshl_b32 s4, s5, 6
	s_mulk_i32 s5, 0xcfc0
	s_add_i32 s14, s2, s5
	v_or_b32_e32 v1, s4, v8
	v_or_b32_e32 v34, s4, v9
	v_or_b32_e32 v36, s4, v10
	v_or_b32_e32 v38, s4, v11
	v_or_b32_e32 v40, s4, v12
	v_or_b32_e32 v42, s4, v13
	v_or_b32_e32 v44, s4, v14
	v_or_b32_e32 v46, s4, v15
	s_ashr_i32 s15, s14, 31
	v_mad_i64_i32 v[32:33], s[16:17], v1, s11, v[4:5]
	v_mad_i64_i32 v[34:35], s[16:17], v34, s11, v[4:5]
	v_mad_i64_i32 v[36:37], s[16:17], v36, s11, v[4:5]
	v_mad_i64_i32 v[38:39], s[16:17], v38, s11, v[4:5]
	v_mad_i64_i32 v[40:41], s[16:17], v40, s11, v[4:5]
	v_mad_i64_i32 v[42:43], s[16:17], v42, s11, v[4:5]
	v_mad_i64_i32 v[44:45], s[16:17], v44, s11, v[4:5]
	v_mad_i64_i32 v[46:47], s[16:17], v46, s11, v[4:5]
	s_lshl_b64 s[16:17], s[14:15], 2
	s_nop 0
	v_lshl_add_u64 v[32:33], v[32:33], 0, s[16:17]
	v_lshl_add_u64 v[34:35], v[34:35], 0, s[16:17]
	v_lshl_add_u64 v[36:37], v[36:37], 0, s[16:17]
	v_lshl_add_u64 v[38:39], v[38:39], 0, s[16:17]
	v_lshl_add_u64 v[40:41], v[40:41], 0, s[16:17]
	v_lshl_add_u64 v[42:43], v[42:43], 0, s[16:17]
	v_lshl_add_u64 v[44:45], v[44:45], 0, s[16:17]
	v_lshl_add_u64 v[46:47], v[46:47], 0, s[16:17]
	v_lshl_add_u64 v[32:33], v[32:33], 0, v[2:3]
	v_lshl_add_u64 v[48:49], v[34:35], 0, v[2:3]
	v_lshl_add_u64 v[50:51], v[36:37], 0, v[2:3]
	v_lshl_add_u64 v[52:53], v[38:39], 0, v[2:3]
	v_lshl_add_u64 v[54:55], v[40:41], 0, v[2:3]
	v_lshl_add_u64 v[56:57], v[42:43], 0, v[2:3]
	v_lshl_add_u64 v[58:59], v[44:45], 0, v[2:3]
	v_lshl_add_u64 v[60:61], v[46:47], 0, v[2:3]
	global_load_dwordx4 v[110:113], v[32:33], off
	s_nop 0
	global_load_dwordx4 v[114:117], v[48:49], off
	global_load_dwordx4 v[118:121], v[50:51], off
	global_load_dwordx4 v[122:125], v[52:53], off
	s_nop 0
	global_load_dwordx4 v[126:129], v[54:55], off
	s_nop 0
	global_load_dwordx4 v[130:133], v[56:57], off
	s_nop 0
	global_load_dwordx4 v[134:137], v[58:59], off
	s_nop 0
	global_load_dwordx4 v[138:141], v[60:61], off
.Lp0i_nopf:
	s_waitcnt lgkmcnt(0)
	ds_read2_b32 v[34:35], v16 offset0:33 offset1:41
	ds_read2_b32 v[36:37], v16 offset1:8
	ds_read2_b32 v[38:39], v16 offset0:66 offset1:74
	ds_read2_b32 v[40:41], v16 offset0:99 offset1:107
	ds_read2_b32 v[42:43], v16 offset0:132 offset1:140
	ds_read2_b32 v[44:45], v16 offset0:165 offset1:173
	ds_read2_b32 v[46:47], v16 offset0:198 offset1:206
	ds_read2_b32 v[48:49], v16 offset0:231 offset1:239
	ds_read2_b32 v[50:51], v16 offset0:49 offset1:57
	ds_read2_b32 v[52:53], v16 offset0:16 offset1:24
	ds_read2_b32 v[54:55], v16 offset0:82 offset1:90
	ds_read2_b32 v[56:57], v16 offset0:115 offset1:123
	ds_read2_b32 v[58:59], v16 offset0:148 offset1:156
	ds_read2_b32 v[60:61], v16 offset0:181 offset1:189
	ds_read2_b32 v[62:63], v16 offset0:214 offset1:222
	ds_read2_b32 v[72:73], v16 offset0:247 offset1:255
	s_waitcnt lgkmcnt(14)
	v_cvt_pk_bf16_f32 v32, v36, v34
	s_waitcnt lgkmcnt(12)
	v_cvt_pk_bf16_f32 v33, v38, v40
	v_cvt_pk_bf16_f32 v36, v37, v35
	s_waitcnt lgkmcnt(10)
	v_cvt_pk_bf16_f32 v34, v42, v44
	s_waitcnt lgkmcnt(8)
	v_cvt_pk_bf16_f32 v35, v46, v48
	v_cvt_pk_bf16_f32 v37, v39, v41
	v_cvt_pk_bf16_f32 v38, v43, v45
	v_cvt_pk_bf16_f32 v39, v47, v49
	s_waitcnt lgkmcnt(6)
	v_cvt_pk_bf16_f32 v40, v52, v50
	s_waitcnt lgkmcnt(4)
	v_cvt_pk_bf16_f32 v41, v54, v56
	v_cvt_pk_bf16_f32 v44, v53, v51
	v_cvt_pk_bf16_f32 v45, v55, v57
	s_waitcnt lgkmcnt(2)
	v_cvt_pk_bf16_f32 v42, v58, v60
	v_cvt_pk_bf16_f32 v46, v59, v61
	s_waitcnt lgkmcnt(0)
	v_cvt_pk_bf16_f32 v43, v62, v72
	v_cvt_pk_bf16_f32 v47, v63, v73
	global_store_dwordx4 v[64:65], v[32:35], off
	global_store_dwordx4 v[66:67], v[36:39], off
	global_store_dwordx4 v[68:69], v[40:43], off
	global_store_dwordx4 v[70:71], v[44:47], off
	s_waitcnt lgkmcnt(0)
	s_cmp_lg_u32 s18, 0
	s_cbranch_scc0 .LBB0_10
